# v24 + expert-down GEMM epilogue: all eight gate loads of a unit issued together, counted vmcnt per step instead of a load->vmcnt(0)->store ladder
# speedup vs baseline: 1.0195x; 1.0020x over previous
.LBB0_732:
	v_lshl_add_u32 v148, s54, 8, v136
	v_ashrrev_i32_e32 v149, 31, v148
	v_lshl_add_u64 v[132:133], v[148:149], 2, s[18:19]
	global_load_dword v147, v[132:133], off
	global_load_dword v200, v[132:133], off offset:64
	global_load_dword v201, v[132:133], off offset:128
	global_load_dword v202, v[132:133], off offset:192
	global_load_dword v203, v[132:133], off offset:512
	global_load_dword v204, v[132:133], off offset:576
	global_load_dword v205, v[132:133], off offset:640
	global_load_dword v206, v[132:133], off offset:704
	s_lshl_b32 s53, s53, 8
	s_and_b32 s53, s53, 0x300
	v_add_u32_e32 v134, s53, v138
	v_lshlrev_b64 v[152:153], 11, v[148:149]
	v_ashrrev_i32_e32 v135, 31, v134
	v_lshl_add_u64 v[152:153], s[16:17], 0, v[152:153]
	v_lshlrev_b64 v[156:157], 1, v[134:135]
	v_lshl_add_u64 v[134:135], v[152:153], 0, v[156:157]
	v_or_b32_e32 v150, 16, v148
	v_ashrrev_i32_e32 v151, 31, v150
	v_lshl_add_u64 v[154:155], v[150:151], 2, s[18:19]
	s_waitcnt vmcnt(7)
	v_mul_f32_e32 v152, 0x3c1a90e8, v147
	v_pk_mul_f32 v[114:115], v[114:115], v[152:153] op_sel_hi:[1,0]
	v_pk_mul_f32 v[112:113], v[112:113], v[152:153] op_sel_hi:[1,0]
	v_pk_mul_f32 v[118:119], v[118:119], v[152:153] op_sel_hi:[1,0]
	v_pk_mul_f32 v[116:117], v[116:117], v[152:153] op_sel_hi:[1,0]
	v_cvt_pk_bf16_f32 v112, v112, v113
	v_cvt_pk_bf16_f32 v113, v114, v115
	v_cvt_pk_bf16_f32 v115, v118, v119
	v_pk_mul_f32 v[122:123], v[122:123], v[152:153] op_sel_hi:[1,0]
	v_cvt_pk_bf16_f32 v114, v116, v117
	v_pk_mul_f32 v[120:121], v[120:121], v[152:153] op_sel_hi:[1,0]
	v_pk_mul_f32 v[126:127], v[126:127], v[152:153] op_sel_hi:[1,0]
	v_pk_mul_f32 v[124:125], v[124:125], v[152:153] op_sel_hi:[1,0]
	v_cvt_pk_bf16_f32 v116, v120, v121
	v_cvt_pk_bf16_f32 v117, v122, v123
	v_cvt_pk_bf16_f32 v119, v126, v127
	s_nop 0
	v_cvt_pk_bf16_f32 v118, v124, v125
	global_store_dwordx4 v[134:135], v[112:115], off
	global_store_dwordx4 v[134:135], v[116:119], off offset:256
	v_lshlrev_b64 v[114:115], 11, v[150:151]
	v_or_b32_e32 v112, 32, v148
	v_lshl_add_u64 v[114:115], s[16:17], 0, v[114:115]
	v_ashrrev_i32_e32 v113, 31, v112
	v_lshl_add_u64 v[114:115], v[114:115], 0, v[156:157]
	v_lshl_add_u64 v[116:117], v[112:113], 2, s[18:19]
	s_waitcnt vmcnt(8)
	v_mul_f32_e32 v118, 0x3c1a90e8, v200
	v_pk_mul_f32 v[120:121], v[98:99], v[118:119] op_sel_hi:[1,0]
	v_pk_mul_f32 v[98:99], v[96:97], v[118:119] op_sel_hi:[1,0]
	v_pk_mul_f32 v[102:103], v[102:103], v[118:119] op_sel_hi:[1,0]
	v_pk_mul_f32 v[100:101], v[100:101], v[118:119] op_sel_hi:[1,0]
	v_cvt_pk_bf16_f32 v97, v102, v103
	v_cvt_pk_bf16_f32 v98, v98, v99
	v_cvt_pk_bf16_f32 v99, v120, v121
	v_pk_mul_f32 v[110:111], v[110:111], v[118:119] op_sel_hi:[1,0]
	v_cvt_pk_bf16_f32 v96, v100, v101
	v_pk_mul_f32 v[108:109], v[108:109], v[118:119] op_sel_hi:[1,0]
	v_pk_mul_f32 v[106:107], v[106:107], v[118:119] op_sel_hi:[1,0]
	v_pk_mul_f32 v[104:105], v[104:105], v[118:119] op_sel_hi:[1,0]
	v_cvt_pk_bf16_f32 v100, v108, v109
	v_cvt_pk_bf16_f32 v101, v110, v111
	v_cvt_pk_bf16_f32 v103, v106, v107
	s_nop 0
	v_cvt_pk_bf16_f32 v102, v104, v105
	global_store_dwordx4 v[114:115], v[96:99], off
	global_store_dwordx4 v[114:115], v[100:103], off offset:256
	v_lshlrev_b64 v[98:99], 11, v[112:113]
	v_or_b32_e32 v96, 48, v148
	v_lshl_add_u64 v[98:99], s[16:17], 0, v[98:99]
	v_ashrrev_i32_e32 v97, 31, v96
	v_lshl_add_u64 v[98:99], v[98:99], 0, v[156:157]
	v_lshl_add_u64 v[100:101], v[96:97], 2, s[18:19]
	s_waitcnt vmcnt(9)
	v_mul_f32_e32 v102, 0x3c1a90e8, v201
	v_pk_mul_f32 v[104:105], v[82:83], v[102:103] op_sel_hi:[1,0]
	v_pk_mul_f32 v[82:83], v[80:81], v[102:103] op_sel_hi:[1,0]
	v_pk_mul_f32 v[86:87], v[86:87], v[102:103] op_sel_hi:[1,0]
	v_pk_mul_f32 v[84:85], v[84:85], v[102:103] op_sel_hi:[1,0]
	v_cvt_pk_bf16_f32 v81, v86, v87
	v_cvt_pk_bf16_f32 v82, v82, v83
	v_cvt_pk_bf16_f32 v83, v104, v105
	v_pk_mul_f32 v[94:95], v[94:95], v[102:103] op_sel_hi:[1,0]
	v_cvt_pk_bf16_f32 v80, v84, v85
	v_pk_mul_f32 v[92:93], v[92:93], v[102:103] op_sel_hi:[1,0]
	v_pk_mul_f32 v[90:91], v[90:91], v[102:103] op_sel_hi:[1,0]
	v_pk_mul_f32 v[88:89], v[88:89], v[102:103] op_sel_hi:[1,0]
	v_cvt_pk_bf16_f32 v84, v92, v93
	v_cvt_pk_bf16_f32 v85, v94, v95
	v_cvt_pk_bf16_f32 v87, v90, v91
	s_nop 0
	v_cvt_pk_bf16_f32 v86, v88, v89
	global_store_dwordx4 v[98:99], v[80:83], off
	global_store_dwordx4 v[98:99], v[84:87], off offset:256
	v_lshlrev_b64 v[80:81], 11, v[96:97]
	v_lshl_add_u64 v[80:81], s[16:17], 0, v[80:81]
	v_lshl_add_u64 v[80:81], v[80:81], 0, v[156:157]
	s_waitcnt vmcnt(10)
	v_mul_f32_e32 v82, 0x3c1a90e8, v202
	v_pk_mul_f32 v[78:79], v[78:79], v[82:83] op_sel_hi:[1,0]
	v_pk_mul_f32 v[76:77], v[76:77], v[82:83] op_sel_hi:[1,0]
	v_pk_mul_f32 v[74:75], v[74:75], v[82:83] op_sel_hi:[1,0]
	v_pk_mul_f32 v[72:73], v[72:73], v[82:83] op_sel_hi:[1,0]
	v_pk_mul_f32 v[70:71], v[70:71], v[82:83] op_sel_hi:[1,0]
	v_pk_mul_f32 v[68:69], v[68:69], v[82:83] op_sel_hi:[1,0]
	v_pk_mul_f32 v[84:85], v[62:63], v[82:83] op_sel_hi:[1,0]
	v_pk_mul_f32 v[82:83], v[60:61], v[82:83] op_sel_hi:[1,0]
	v_cvt_pk_bf16_f32 v60, v76, v77
	v_cvt_pk_bf16_f32 v61, v78, v79
	v_cvt_pk_bf16_f32 v62, v72, v73
	v_cvt_pk_bf16_f32 v63, v74, v75
	v_cvt_pk_bf16_f32 v68, v68, v69
	v_cvt_pk_bf16_f32 v69, v70, v71
	s_nop 0
	v_cvt_pk_bf16_f32 v70, v82, v83
	v_cvt_pk_bf16_f32 v71, v84, v85
	global_store_dwordx4 v[80:81], v[60:63], off
	global_store_dwordx4 v[80:81], v[68:71], off offset:256
	v_add_co_u32_e32 v62, vcc, s47, v134
	v_lshl_add_u64 v[60:61], v[134:135], 0, s[22:23]
	s_nop 0
	v_addc_co_u32_e32 v63, vcc, 0, v135, vcc
	s_waitcnt vmcnt(11)
	v_mul_f32_e32 v68, 0x3c1a90e8, v203
	v_pk_mul_f32 v[70:71], v[50:51], v[68:69] op_sel_hi:[1,0]
	v_pk_mul_f32 v[50:51], v[48:49], v[68:69] op_sel_hi:[1,0]
	v_pk_mul_f32 v[54:55], v[54:55], v[68:69] op_sel_hi:[1,0]
	v_pk_mul_f32 v[52:53], v[52:53], v[68:69] op_sel_hi:[1,0]
	v_cvt_pk_bf16_f32 v49, v54, v55
	v_cvt_pk_bf16_f32 v50, v50, v51
	v_cvt_pk_bf16_f32 v51, v70, v71
	v_pk_mul_f32 v[66:67], v[66:67], v[68:69] op_sel_hi:[1,0]
	v_cvt_pk_bf16_f32 v48, v52, v53
	v_pk_mul_f32 v[64:65], v[64:65], v[68:69] op_sel_hi:[1,0]
	v_pk_mul_f32 v[58:59], v[58:59], v[68:69] op_sel_hi:[1,0]
	v_pk_mul_f32 v[56:57], v[56:57], v[68:69] op_sel_hi:[1,0]
	v_cvt_pk_bf16_f32 v52, v64, v65
	v_cvt_pk_bf16_f32 v53, v66, v67
	v_cvt_pk_bf16_f32 v55, v58, v59
	s_nop 0
	v_cvt_pk_bf16_f32 v54, v56, v57
	global_store_dwordx4 v[62:63], v[48:51], off
	global_store_dwordx4 v[60:61], v[52:55], off offset:256
	v_add_co_u32_e32 v50, vcc, s48, v134
	v_lshl_add_u64 v[48:49], v[134:135], 0, s[24:25]
	s_nop 0
	v_addc_co_u32_e32 v51, vcc, 0, v135, vcc
	s_waitcnt vmcnt(12)
	v_mul_f32_e32 v52, 0x3c1a90e8, v204
	v_pk_mul_f32 v[54:55], v[34:35], v[52:53] op_sel_hi:[1,0]
	v_pk_mul_f32 v[34:35], v[32:33], v[52:53] op_sel_hi:[1,0]
	v_pk_mul_f32 v[38:39], v[38:39], v[52:53] op_sel_hi:[1,0]
	v_pk_mul_f32 v[36:37], v[36:37], v[52:53] op_sel_hi:[1,0]
	v_cvt_pk_bf16_f32 v33, v38, v39
	v_cvt_pk_bf16_f32 v34, v34, v35
	v_cvt_pk_bf16_f32 v35, v54, v55
	v_pk_mul_f32 v[46:47], v[46:47], v[52:53] op_sel_hi:[1,0]
	v_cvt_pk_bf16_f32 v32, v36, v37
	v_pk_mul_f32 v[44:45], v[44:45], v[52:53] op_sel_hi:[1,0]
	v_pk_mul_f32 v[42:43], v[42:43], v[52:53] op_sel_hi:[1,0]
	v_pk_mul_f32 v[40:41], v[40:41], v[52:53] op_sel_hi:[1,0]
	v_cvt_pk_bf16_f32 v36, v44, v45
	v_cvt_pk_bf16_f32 v37, v46, v47
	v_cvt_pk_bf16_f32 v39, v42, v43
	s_nop 0
	v_cvt_pk_bf16_f32 v38, v40, v41
	global_store_dwordx4 v[50:51], v[32:35], off
	global_store_dwordx4 v[48:49], v[36:39], off offset:256
	v_add_co_u32_e32 v34, vcc, s49, v134
	v_lshl_add_u64 v[32:33], v[134:135], 0, s[26:27]
	s_nop 0
	v_addc_co_u32_e32 v35, vcc, 0, v135, vcc
	s_andn2_b64 vcc, exec, s[0:1]
	s_waitcnt vmcnt(13)
	v_mul_f32_e32 v36, 0x3c1a90e8, v205
	v_pk_mul_f32 v[38:39], v[18:19], v[36:37] op_sel_hi:[1,0]
	v_pk_mul_f32 v[18:19], v[16:17], v[36:37] op_sel_hi:[1,0]
	v_pk_mul_f32 v[26:27], v[26:27], v[36:37] op_sel_hi:[1,0]
	v_pk_mul_f32 v[24:25], v[24:25], v[36:37] op_sel_hi:[1,0]
	v_pk_mul_f32 v[40:41], v[22:23], v[36:37] op_sel_hi:[1,0]
	v_pk_mul_f32 v[22:23], v[20:21], v[36:37] op_sel_hi:[1,0]
	v_cvt_pk_bf16_f32 v16, v24, v25
	v_cvt_pk_bf16_f32 v17, v26, v27
	v_cvt_pk_bf16_f32 v18, v18, v19
	v_cvt_pk_bf16_f32 v19, v38, v39
	v_pk_mul_f32 v[30:31], v[30:31], v[36:37] op_sel_hi:[1,0]
	v_pk_mul_f32 v[28:29], v[28:29], v[36:37] op_sel_hi:[1,0]
	v_cvt_pk_bf16_f32 v21, v30, v31
	v_cvt_pk_bf16_f32 v22, v22, v23
	v_cvt_pk_bf16_f32 v23, v40, v41
	s_nop 0
	v_cvt_pk_bf16_f32 v20, v28, v29
	global_store_dwordx4 v[34:35], v[16:19], off
	global_store_dwordx4 v[32:33], v[20:23], off offset:256
	v_add_co_u32_e64 v18, s[0:1], s50, v134
	v_lshl_add_u64 v[16:17], v[134:135], 0, s[28:29]
	s_nop 0
	v_addc_co_u32_e64 v19, s[0:1], 0, v135, s[0:1]
	s_mov_b64 s[0:1], -1
	s_waitcnt vmcnt(14)
	v_mul_f32_e32 v20, 0x3c1a90e8, v206
	v_pk_mul_f32 v[22:23], v[2:3], v[20:21] op_sel_hi:[1,0]
	v_pk_mul_f32 v[2:3], v[0:1], v[20:21] op_sel_hi:[1,0]
	v_pk_mul_f32 v[6:7], v[6:7], v[20:21] op_sel_hi:[1,0]
	v_pk_mul_f32 v[4:5], v[4:5], v[20:21] op_sel_hi:[1,0]
	v_cvt_pk_bf16_f32 v1, v6, v7
	v_cvt_pk_bf16_f32 v2, v2, v3
	v_cvt_pk_bf16_f32 v3, v22, v23
	v_pk_mul_f32 v[14:15], v[14:15], v[20:21] op_sel_hi:[1,0]
	v_cvt_pk_bf16_f32 v0, v4, v5
	v_pk_mul_f32 v[12:13], v[12:13], v[20:21] op_sel_hi:[1,0]
	v_pk_mul_f32 v[10:11], v[10:11], v[20:21] op_sel_hi:[1,0]
	v_pk_mul_f32 v[8:9], v[8:9], v[20:21] op_sel_hi:[1,0]
	v_cvt_pk_bf16_f32 v4, v12, v13
	v_cvt_pk_bf16_f32 v5, v14, v15
	v_cvt_pk_bf16_f32 v7, v10, v11
	s_nop 0
	v_cvt_pk_bf16_f32 v6, v8, v9
	global_store_dwordx4 v[18:19], v[0:3], off
	global_store_dwordx4 v[16:17], v[4:7], off offset:256
	s_cbranch_vccnz .LBB0_723
	s_andn2_b64 vcc, exec, s[14:15]
	s_cbranch_vccnz .LBB0_722
	s_barrier
	s_branch .LBB0_722
